# agg1: uniform branch skips the masked index-chunk loads for slots 24..39 when the wave's largest degree is at most 24
# baseline (speedup 1.0000x reference)
_Z11agg1_kernelPKDF16_PKfS2_PKiS4_S2_S2_PDF16_PfS6_i:
	s_load_dwordx8 s[4:11], s[0:1], 0x0
	s_load_dwordx8 s[12:19], s[0:1], 0x20
	s_load_dwordx4 s[20:23], s[0:1], 0x40
	s_load_dword s24, s[0:1], 0x50
	v_lshlrev_b32_e32 v32, 2, v0
	v_readfirstlane_b32 s25, v0
	s_lshl_b32 s26, s2, 5
	v_and_b32_e32 v64, 7, v0
	v_bfe_u32 v65, v0, 3, 3
	v_and_b32_e32 v45, 31, v0
	s_lshr_b32 s25, s25, 6
	s_getreg_b32 s30, hwreg(HW_REG_HW_ID, 4, 2)
	s_lshr_b32 s31, s2, 8
	s_lshl_b32 s31, s31, 3
	s_mov_b32 s44, 0x276c9c8d
	s_mov_b32 s45, 0xe46393
	s_and_b32 s47, s2, 0xff
	s_cmp_lt_u32 s47, 27
	s_cselect_b32 s44, 0xb1784b63, s44
	s_cselect_b32 s45, 0x1e4ee4, s45
	s_lshr_b64 s[44:45], s[44:45], s31
	s_lshl_b32 s31, s30, 1
	s_lshr_b32 s44, s44, s31
	s_and_b32 s44, s44, 3
	s_lshl_b32 s45, 1, s30
	s_lshl_b32 s46, s25, 2
	s_addk_i32 s46, 0x2800
	v_mov_b32_e32 v49, s45
	v_mov_b32_e32 v50, s46
	ds_write_b32 v50, v49
	v_lshlrev_b32_e32 v1, 1, v64
	v_add_u32_e32 v46, s26, v45
	s_waitcnt lgkmcnt(0)
	global_load_dword v33, v32, s[14:15]
	global_load_dword v34, v32, s[16:17]
	s_add_i32 s28, s24, -1
	v_cmp_gt_i32_e64 s[38:39], s24, v46
	v_min_i32_e32 v46, s28, v46
	v_lshlrev_b32_e32 v47, 2, v46
	global_load_dword v44, v47, s[10:11]
	global_load_dword v48, v47, s[10:11] offset:4
	s_lshl_b32 s27, s25, 11
	v_lshlrev_b32_e32 v62, 6, v64
	v_add_u32_e32 v62, 0x2000, v62
	v_cmp_eq_u32_e64 s[34:35], 0, v64
	v_lshlrev_b32_e32 v35, 8, v64
	v_lshl_add_u32 v35, v65, 4, v35
	v_add_u32_e32 v63, s27, v35
	v_mov_b32_e32 v36, 0
	v_mov_b32_e32 v37, 0
	v_mov_b32_e32 v38, 0
	v_mov_b32_e32 v39, 0
	s_waitcnt vmcnt(2)
	ds_write2st64_b32 v32, v33, v34 offset0:32 offset1:36
	ds_write_b128 v63, v[36:39]
	ds_write_b128 v63, v[36:39] offset:128
	s_waitcnt vmcnt(0)
	v_sub_u32_e32 v48, v48, v44
	v_add_u32_e32 v48, 1, v48
	v_cndmask_b32_e64 v48, 0, v48, s[38:39]
	v_lshl_or_b32 v40, v48, 5, v45
	s_lshl_b32 s31, s25, 2
	s_addk_i32 s31, 0x2810
	s_lshl_b32 s47, s25, 3
	v_mov_b32_e32 v41, 0
	s_nop 1
	v_readlane_b32 s46, v40, s47
	s_add_i32 s47, s47, 1
	v_cmp_gt_u32_e32 vcc, s46, v40
	v_addc_co_u32_e32 v41, vcc, 0, v41, vcc
	v_readlane_b32 s46, v40, s47
	s_add_i32 s47, s47, 1
	v_cmp_gt_u32_e32 vcc, s46, v40
	v_addc_co_u32_e32 v41, vcc, 0, v41, vcc
	v_readlane_b32 s46, v40, s47
	s_add_i32 s47, s47, 1
	v_cmp_gt_u32_e32 vcc, s46, v40
	v_addc_co_u32_e32 v41, vcc, 0, v41, vcc
	v_readlane_b32 s46, v40, s47
	s_add_i32 s47, s47, 1
	v_cmp_gt_u32_e32 vcc, s46, v40
	v_addc_co_u32_e32 v41, vcc, 0, v41, vcc
	v_readlane_b32 s46, v40, s47
	s_add_i32 s47, s47, 1
	v_cmp_gt_u32_e32 vcc, s46, v40
	v_addc_co_u32_e32 v41, vcc, 0, v41, vcc
	v_readlane_b32 s46, v40, s47
	s_add_i32 s47, s47, 1
	v_cmp_gt_u32_e32 vcc, s46, v40
	v_addc_co_u32_e32 v41, vcc, 0, v41, vcc
	v_readlane_b32 s46, v40, s47
	s_add_i32 s47, s47, 1
	v_cmp_gt_u32_e32 vcc, s46, v40
	v_addc_co_u32_e32 v41, vcc, 0, v41, vcc
	v_readlane_b32 s46, v40, s47
	s_add_i32 s47, s47, 1
	v_cmp_gt_u32_e32 vcc, s46, v40
	v_addc_co_u32_e32 v41, vcc, 0, v41, vcc
	v_lshl_add_u32 v42, v45, 4, s31
	ds_write_b32 v42, v41
	v_mov_b32_e32 v50, 0x2800
	s_waitcnt lgkmcnt(0)
	s_barrier
	ds_read_b128 v[52:55], v50
	v_lshlrev_b32_e32 v42, 4, v45
	ds_read_b128 v[48:51], v42 offset:10256
	s_waitcnt lgkmcnt(1)
	v_or3_b32 v52, v52, v53, v54
	v_or_b32_e32 v52, v52, v55
	s_nop 0
	v_readfirstlane_b32 s46, v52
	s_cmp_eq_u32 s46, 15
	s_cselect_b32 s44, s44, s25
	s_lshl_b32 s40, s44, 3
	s_waitcnt lgkmcnt(0)
	v_add3_u32 v48, v48, v49, v50
	v_add_u32_e32 v48, v48, v51
	v_lshlrev_b32_e32 v48, 2, v48
	ds_permute_b32 v40, v48, v40
	v_add_u32_e32 v45, s40, v65
	v_lshlrev_b32_e32 v45, 2, v45
	s_waitcnt lgkmcnt(0)
	ds_bpermute_b32 v46, v45, v40
	s_waitcnt lgkmcnt(0)
	v_and_b32_e32 v15, 31, v46
	v_lshrrev_b32_e32 v11, 5, v46
	v_lshlrev_b32_e32 v47, 2, v15
	ds_bpermute_b32 v10, v47, v44
	v_add_u32_e32 v66, s26, v15
	v_min_i32_e32 v66, s28, v66
	v_cmp_lt_u32_e64 s[36:37], 0, v11
	v_lshlrev_b32_e32 v4, 2, v66
	v_lshlrev_b32_e32 v35, 2, v64
	v_lshl_or_b32 v35, v66, 5, v35
	global_load_dword v9, v35, s[8:9]
	v_lshrrev_b32_e32 v3, 3, v15
	v_lshlrev_b32_e32 v3, 11, v3
	v_and_b32_e32 v47, 7, v15
	v_lshl_add_u32 v3, v47, 1, v3
	v_lshl_add_u32 v3, v64, 4, v3
	v_readfirstlane_b32 s29, v11
	s_waitcnt lgkmcnt(0)
	v_add_u32_e32 v67, v10, v64
	v_lshlrev_b32_e32 v67, 2, v67
	v_mov_b32_e32 v5, s24
	v_mov_b32_e32 v6, s24
	v_mov_b32_e32 v7, s24
	v_mov_b32_e32 v8, s24
	v_mov_b32_e32 v69, s24
	v_cndmask_b32_e64 v5, v5, v66, s[34:35]
	v_cmp_gt_i32_e32 vcc, v11, v64
	s_andn2_b64 s[40:41], vcc, s[34:35]
	s_and_saveexec_b64 s[32:33], s[40:41]
	global_load_dword v5, v67, s[12:13] offset:-4
	s_mov_b64 exec, s[32:33]
	v_add_u32_e32 v68, 8, v64
	v_cmp_gt_i32_e32 vcc, v11, v68
	s_and_saveexec_b64 s[32:33], vcc
	global_load_dword v6, v67, s[12:13] offset:28
	s_mov_b64 exec, s[32:33]
	v_add_u32_e32 v68, 16, v64
	v_cmp_gt_i32_e32 vcc, v11, v68
	s_and_saveexec_b64 s[32:33], vcc
	global_load_dword v7, v67, s[12:13] offset:60
	s_mov_b64 exec, s[32:33]
	s_cmp_lt_i32 s29, 25
	s_cbranch_scc1 .Lagg_idx_short
	v_add_u32_e32 v68, 24, v64
	v_cmp_gt_i32_e32 vcc, v11, v68
	s_and_saveexec_b64 s[32:33], vcc
	global_load_dword v8, v67, s[12:13] offset:92
	s_mov_b64 exec, s[32:33]
	v_add_u32_e32 v68, 32, v64
	v_cmp_gt_i32_e32 vcc, v11, v68
	s_and_saveexec_b64 s[32:33], vcc
	global_load_dword v69, v67, s[12:13] offset:124
	s_mov_b64 exec, s[32:33]
.Lagg_idx_short:
	s_waitcnt vmcnt(0)
	v_lshlrev_b32_e32 v5, 4, v5
	v_lshlrev_b32_e32 v6, 4, v6
	v_lshlrev_b32_e32 v7, 4, v7
	v_lshlrev_b32_e32 v8, 4, v8
	v_lshlrev_b32_e32 v69, 4, v69
	s_mov_b32 s42, 0
	s_mov_b32 s43, 0
	ds_swizzle_b32 v32, v5 offset:swizzle(BITMASK_PERM, "pp000")
	ds_swizzle_b32 v33, v5 offset:swizzle(BITMASK_PERM, "pp001")
	ds_swizzle_b32 v34, v5 offset:swizzle(BITMASK_PERM, "pp010")
	ds_swizzle_b32 v35, v5 offset:swizzle(BITMASK_PERM, "pp011")
	s_cmp_lt_i32 s29, 3
	s_cbranch_scc1 .Lagg_first_half
	s_waitcnt lgkmcnt(0)
	v_or_b32_e32 v32, v32, v1
	v_or_b32_e32 v33, v33, v1
	v_or_b32_e32 v34, v34, v1
	v_or_b32_e32 v35, v35, v1
	global_load_ushort v36, v32, s[6:7]
	global_load_ushort v37, v33, s[6:7]
	global_load_ushort v38, v34, s[6:7]
	global_load_ushort v39, v35, s[6:7]
	v_lshlrev_b32_e32 v32, 3, v32
	v_lshlrev_b32_e32 v33, 3, v33
	v_lshlrev_b32_e32 v34, 3, v34
	v_lshlrev_b32_e32 v35, 3, v35
	global_load_dwordx4 v[40:43], v32, s[4:5]
	global_load_dwordx4 v[44:47], v33, s[4:5]
	global_load_dwordx4 v[48:51], v34, s[4:5]
	global_load_dwordx4 v[52:55], v35, s[4:5]
	ds_swizzle_b32 v32, v5 offset:swizzle(BITMASK_PERM, "pp100")
	ds_swizzle_b32 v33, v5 offset:swizzle(BITMASK_PERM, "pp101")
	ds_swizzle_b32 v34, v5 offset:swizzle(BITMASK_PERM, "pp110")
	ds_swizzle_b32 v35, v5 offset:swizzle(BITMASK_PERM, "pp111")
	s_waitcnt vmcnt(4)
	v_fma_mix_f32 v36, v36, 1.0, v9 op_sel_hi:[1,0,0]
	v_fma_mix_f32 v37, v37, 1.0, v9 op_sel_hi:[1,0,0]
	v_fma_mix_f32 v38, v38, 1.0, v9 op_sel_hi:[1,0,0]
	v_fma_mix_f32 v39, v39, 1.0, v9 op_sel_hi:[1,0,0]
	v_mul_f32_e32 v58, 0x3e4ccccd, v36
	v_mul_f32_e32 v59, 0x3e4ccccd, v37
	v_mul_f32_e32 v60, 0x3e4ccccd, v38
	v_mul_f32_e32 v61, 0x3e4ccccd, v39
	v_max_f32_e32 v36, v36, v58
	v_max_f32_e32 v37, v37, v59
	v_max_f32_e32 v38, v38, v60
	v_max_f32_e32 v39, v39, v61
	v_max3_f32 v56, v36, v37, v38
	v_max_f32_e32 v13, v56, v39
	v_sub_f32_e32 v36, v36, v13
	v_sub_f32_e32 v37, v37, v13
	v_sub_f32_e32 v38, v38, v13
	v_sub_f32_e32 v39, v39, v13
	v_exp_f32_e32 v36, v36
	v_exp_f32_e32 v37, v37
	v_exp_f32_e32 v38, v38
	v_exp_f32_e32 v39, v39
	s_nop 0
	v_add_f32_e32 v14, v36, v37
	v_add_f32_e32 v14, v14, v38
	v_add_f32_e32 v14, v14, v39
	s_waitcnt vmcnt(3)
	v_cvt_scalef32_pk_f16_fp8 v58, v40, 1.0
	v_cvt_scalef32_pk_f16_fp8 v59, v40, 1.0 op_sel:[1,0,0]
	v_cvt_scalef32_pk_f16_fp8 v60, v41, 1.0
	v_cvt_scalef32_pk_f16_fp8 v61, v41, 1.0 op_sel:[1,0,0]
	v_fma_mix_f32 v16, v58, v36, 0 op_sel_hi:[1,0,0]
	v_fma_mix_f32 v17, v58, v36, 0 op_sel:[1,0,0] op_sel_hi:[1,0,0]
	v_fma_mix_f32 v18, v59, v36, 0 op_sel_hi:[1,0,0]
	v_fma_mix_f32 v19, v59, v36, 0 op_sel:[1,0,0] op_sel_hi:[1,0,0]
	v_fma_mix_f32 v20, v60, v36, 0 op_sel_hi:[1,0,0]
	v_fma_mix_f32 v21, v60, v36, 0 op_sel:[1,0,0] op_sel_hi:[1,0,0]
	v_fma_mix_f32 v22, v61, v36, 0 op_sel_hi:[1,0,0]
	v_fma_mix_f32 v23, v61, v36, 0 op_sel:[1,0,0] op_sel_hi:[1,0,0]
	v_cvt_scalef32_pk_f16_fp8 v58, v42, 1.0
	v_cvt_scalef32_pk_f16_fp8 v59, v42, 1.0 op_sel:[1,0,0]
	v_cvt_scalef32_pk_f16_fp8 v60, v43, 1.0
	v_cvt_scalef32_pk_f16_fp8 v61, v43, 1.0 op_sel:[1,0,0]
	v_fma_mix_f32 v24, v58, v36, 0 op_sel_hi:[1,0,0]
	v_fma_mix_f32 v25, v58, v36, 0 op_sel:[1,0,0] op_sel_hi:[1,0,0]
	v_fma_mix_f32 v26, v59, v36, 0 op_sel_hi:[1,0,0]
	v_fma_mix_f32 v27, v59, v36, 0 op_sel:[1,0,0] op_sel_hi:[1,0,0]
	v_fma_mix_f32 v28, v60, v36, 0 op_sel_hi:[1,0,0]
	v_fma_mix_f32 v29, v60, v36, 0 op_sel:[1,0,0] op_sel_hi:[1,0,0]
	v_fma_mix_f32 v30, v61, v36, 0 op_sel_hi:[1,0,0]
	v_fma_mix_f32 v31, v61, v36, 0 op_sel:[1,0,0] op_sel_hi:[1,0,0]
	s_waitcnt vmcnt(2)
	v_cvt_scalef32_pk_f16_fp8 v58, v44, 1.0
	v_cvt_scalef32_pk_f16_fp8 v59, v44, 1.0 op_sel:[1,0,0]
	v_cvt_scalef32_pk_f16_fp8 v60, v45, 1.0
	v_cvt_scalef32_pk_f16_fp8 v61, v45, 1.0 op_sel:[1,0,0]
	v_fma_mix_f32 v16, v58, v37, v16 op_sel_hi:[1,0,0]
	v_fma_mix_f32 v17, v58, v37, v17 op_sel:[1,0,0] op_sel_hi:[1,0,0]
	v_fma_mix_f32 v18, v59, v37, v18 op_sel_hi:[1,0,0]
	v_fma_mix_f32 v19, v59, v37, v19 op_sel:[1,0,0] op_sel_hi:[1,0,0]
	v_fma_mix_f32 v20, v60, v37, v20 op_sel_hi:[1,0,0]
	v_fma_mix_f32 v21, v60, v37, v21 op_sel:[1,0,0] op_sel_hi:[1,0,0]
	v_fma_mix_f32 v22, v61, v37, v22 op_sel_hi:[1,0,0]
	v_fma_mix_f32 v23, v61, v37, v23 op_sel:[1,0,0] op_sel_hi:[1,0,0]
	v_cvt_scalef32_pk_f16_fp8 v58, v46, 1.0
	v_cvt_scalef32_pk_f16_fp8 v59, v46, 1.0 op_sel:[1,0,0]
	v_cvt_scalef32_pk_f16_fp8 v60, v47, 1.0
	v_cvt_scalef32_pk_f16_fp8 v61, v47, 1.0 op_sel:[1,0,0]
	v_fma_mix_f32 v24, v58, v37, v24 op_sel_hi:[1,0,0]
	v_fma_mix_f32 v25, v58, v37, v25 op_sel:[1,0,0] op_sel_hi:[1,0,0]
	v_fma_mix_f32 v26, v59, v37, v26 op_sel_hi:[1,0,0]
	v_fma_mix_f32 v27, v59, v37, v27 op_sel:[1,0,0] op_sel_hi:[1,0,0]
	v_fma_mix_f32 v28, v60, v37, v28 op_sel_hi:[1,0,0]
	v_fma_mix_f32 v29, v60, v37, v29 op_sel:[1,0,0] op_sel_hi:[1,0,0]
	v_fma_mix_f32 v30, v61, v37, v30 op_sel_hi:[1,0,0]
	v_fma_mix_f32 v31, v61, v37, v31 op_sel:[1,0,0] op_sel_hi:[1,0,0]
	s_waitcnt vmcnt(1)
	v_cvt_scalef32_pk_f16_fp8 v58, v48, 1.0
	v_cvt_scalef32_pk_f16_fp8 v59, v48, 1.0 op_sel:[1,0,0]
	v_cvt_scalef32_pk_f16_fp8 v60, v49, 1.0
	v_cvt_scalef32_pk_f16_fp8 v61, v49, 1.0 op_sel:[1,0,0]
	v_fma_mix_f32 v16, v58, v38, v16 op_sel_hi:[1,0,0]
	v_fma_mix_f32 v17, v58, v38, v17 op_sel:[1,0,0] op_sel_hi:[1,0,0]
	v_fma_mix_f32 v18, v59, v38, v18 op_sel_hi:[1,0,0]
	v_fma_mix_f32 v19, v59, v38, v19 op_sel:[1,0,0] op_sel_hi:[1,0,0]
	v_fma_mix_f32 v20, v60, v38, v20 op_sel_hi:[1,0,0]
	v_fma_mix_f32 v21, v60, v38, v21 op_sel:[1,0,0] op_sel_hi:[1,0,0]
	v_fma_mix_f32 v22, v61, v38, v22 op_sel_hi:[1,0,0]
	v_fma_mix_f32 v23, v61, v38, v23 op_sel:[1,0,0] op_sel_hi:[1,0,0]
	v_cvt_scalef32_pk_f16_fp8 v58, v50, 1.0
	v_cvt_scalef32_pk_f16_fp8 v59, v50, 1.0 op_sel:[1,0,0]
	v_cvt_scalef32_pk_f16_fp8 v60, v51, 1.0
	v_cvt_scalef32_pk_f16_fp8 v61, v51, 1.0 op_sel:[1,0,0]
	v_fma_mix_f32 v24, v58, v38, v24 op_sel_hi:[1,0,0]
	v_fma_mix_f32 v25, v58, v38, v25 op_sel:[1,0,0] op_sel_hi:[1,0,0]
	v_fma_mix_f32 v26, v59, v38, v26 op_sel_hi:[1,0,0]
	v_fma_mix_f32 v27, v59, v38, v27 op_sel:[1,0,0] op_sel_hi:[1,0,0]
	v_fma_mix_f32 v28, v60, v38, v28 op_sel_hi:[1,0,0]
	v_fma_mix_f32 v29, v60, v38, v29 op_sel:[1,0,0] op_sel_hi:[1,0,0]
	v_fma_mix_f32 v30, v61, v38, v30 op_sel_hi:[1,0,0]
	v_fma_mix_f32 v31, v61, v38, v31 op_sel:[1,0,0] op_sel_hi:[1,0,0]
	s_waitcnt vmcnt(0)
	v_cvt_scalef32_pk_f16_fp8 v58, v52, 1.0
	v_cvt_scalef32_pk_f16_fp8 v59, v52, 1.0 op_sel:[1,0,0]
	v_cvt_scalef32_pk_f16_fp8 v60, v53, 1.0
	v_cvt_scalef32_pk_f16_fp8 v61, v53, 1.0 op_sel:[1,0,0]
	v_fma_mix_f32 v16, v58, v39, v16 op_sel_hi:[1,0,0]
	v_fma_mix_f32 v17, v58, v39, v17 op_sel:[1,0,0] op_sel_hi:[1,0,0]
	v_fma_mix_f32 v18, v59, v39, v18 op_sel_hi:[1,0,0]
	v_fma_mix_f32 v19, v59, v39, v19 op_sel:[1,0,0] op_sel_hi:[1,0,0]
	v_fma_mix_f32 v20, v60, v39, v20 op_sel_hi:[1,0,0]
	v_fma_mix_f32 v21, v60, v39, v21 op_sel:[1,0,0] op_sel_hi:[1,0,0]
	v_fma_mix_f32 v22, v61, v39, v22 op_sel_hi:[1,0,0]
	v_fma_mix_f32 v23, v61, v39, v23 op_sel:[1,0,0] op_sel_hi:[1,0,0]
	v_cvt_scalef32_pk_f16_fp8 v58, v54, 1.0
	v_cvt_scalef32_pk_f16_fp8 v59, v54, 1.0 op_sel:[1,0,0]
	v_cvt_scalef32_pk_f16_fp8 v60, v55, 1.0
	v_cvt_scalef32_pk_f16_fp8 v61, v55, 1.0 op_sel:[1,0,0]
	v_fma_mix_f32 v24, v58, v39, v24 op_sel_hi:[1,0,0]
	v_fma_mix_f32 v25, v58, v39, v25 op_sel:[1,0,0] op_sel_hi:[1,0,0]
	v_fma_mix_f32 v26, v59, v39, v26 op_sel_hi:[1,0,0]
	v_fma_mix_f32 v27, v59, v39, v27 op_sel:[1,0,0] op_sel_hi:[1,0,0]
	v_fma_mix_f32 v28, v60, v39, v28 op_sel_hi:[1,0,0]
	v_fma_mix_f32 v29, v60, v39, v29 op_sel:[1,0,0] op_sel_hi:[1,0,0]
	v_fma_mix_f32 v30, v61, v39, v30 op_sel_hi:[1,0,0]
	v_fma_mix_f32 v31, v61, v39, v31 op_sel:[1,0,0] op_sel_hi:[1,0,0]
	s_sub_i32 s29, s29, 4
	s_branch .Lagg_B
